# v45-like with codebook operand loads deferred from kernel start to just before the gather
# speedup vs baseline: 1.0093x; 1.0093x over previous
_Z7vq_mainPKfPKiS0_PfPhPdPi:
	s_load_dwordx4 s[4:7], s[0:1], 0x0
	s_load_dwordx2 s[22:23], s[0:1], 0x10
	s_load_dwordx2 s[20:21], s[0:1], 0x18
	s_load_dwordx4 s[12:15], s[0:1], 0x20
	s_load_dwordx2 s[10:11], s[0:1], 0x30
	s_and_b32 s3, s2, 7
	s_lshl_b32 s3, s3, 6
	s_lshr_b32 s16, s2, 3
	s_add_i32 s16, s16, s3
	s_lshr_b32 s18, s16, 5
	s_mov_b32 s19, 0
	s_and_b32 s28, s16, 31
	s_lshl_b32 s28, s28, 4
	s_add_i32 s29, s28, 1
	v_readfirstlane_b32 s17, v0
	v_and_b32_e32 v1, 63, v0
	v_lshlrev_b32_e32 v66, 4, v0
	s_lshr_b32 s17, s17, 6
	s_lshl_b32 s24, s17, 4
	s_lshl_b32 s30, s18, 15
	s_lshl_b32 s31, s18, 23
	v_add_u32_e32 v67, 0x1000, v66
	v_add_u32_e32 v68, 0x2000, v66
	v_add_u32_e32 v69, 0x3000, v66
	v_add_u32_e32 v70, 0x4000, v66
	v_add_u32_e32 v71, 0x5000, v66
	v_add_u32_e32 v72, 0x6000, v66
	v_add_u32_e32 v73, 0x7000, v66
	s_movk_i32 s9, 0x810
	s_mov_b32 s3, 0x8100
	s_mul_i32 s36, s29, 0x810
	v_mov_b32_e32 v141, s36
	v_sub_u32_e32 v141, 0, v141
	s_waitcnt lgkmcnt(0)
	s_add_u32 s34, s6, s30
	s_addc_u32 s35, s7, 0
	s_add_u32 s32, s4, s31
	s_addc_u32 s33, s5, 0
	global_load_dwordx4 v[74:77], v66, s[34:35]
	global_load_dwordx4 v[78:81], v67, s[34:35]
	global_load_dwordx4 v[82:85], v68, s[34:35]
	global_load_dwordx4 v[86:89], v69, s[34:35]
	global_load_dwordx4 v[90:93], v70, s[34:35]
	global_load_dwordx4 v[94:97], v71, s[34:35]
	global_load_dwordx4 v[98:101], v72, s[34:35]
	global_load_dwordx4 v[102:105], v73, s[34:35]
	v_mov_b32_e32 v142, 1
	v_mov_b32_e32 v143, 4
	v_mov_b32_e32 v144, 0x11100
	v_lshlrev_b32_e32 v145, 8, v0
	v_lshlrev_b32_e32 v148, 3, v0
	v_mov_b32_e32 v152, 0
	v_mov_b32_e32 v153, 0
	ds_write_b64 v148, v[152:153] offset:32768
	ds_write_b64 v148, v[152:153] offset:34832
	ds_write_b64 v148, v[152:153] offset:36896
	ds_write_b64 v148, v[152:153] offset:38960
	ds_write_b64 v148, v[152:153] offset:41024
	ds_write_b64 v148, v[152:153] offset:43088
	ds_write_b64 v148, v[152:153] offset:45152
	ds_write_b64 v148, v[152:153] offset:47216
	ds_write_b64 v148, v[152:153] offset:49280
	ds_write_b64 v148, v[152:153] offset:51344
	ds_write_b64 v148, v[152:153] offset:53408
	ds_write_b64 v148, v[152:153] offset:55472
	ds_write_b64 v148, v[152:153] offset:57536
	ds_write_b64 v148, v[152:153] offset:59600
	ds_write_b64 v148, v[152:153] offset:61664
	ds_write_b64 v148, v[152:153] offset:63728
	v_cmp_gt_u32_e32 vcc, 16, v0
	s_and_saveexec_b64 s[30:31], vcc
	v_mul_u32_u24_e32 v151, 0x810, v0
	ds_write_b64 v151, v[152:153] offset:34816
	v_mov_b32_e32 v150, 0x11540
	v_mov_b32_e32 v149, 8
	ds_write_b32 v150, v149
	s_mov_b64 exec, s[30:31]
	s_waitcnt lgkmcnt(0)
	s_barrier
	s_waitcnt vmcnt(0)
	v_mad_u32_u24 v74, v74, s9, v141
	v_mad_u32_u24 v75, v75, s9, v141
	v_mad_u32_u24 v76, v76, s9, v141
	v_mad_u32_u24 v77, v77, s9, v141
	v_mad_u32_u24 v78, v78, s9, v141
	v_mad_u32_u24 v79, v79, s9, v141
	v_mad_u32_u24 v80, v80, s9, v141
	v_mad_u32_u24 v81, v81, s9, v141
	v_mad_u32_u24 v82, v82, s9, v141
	v_mad_u32_u24 v83, v83, s9, v141
	v_mad_u32_u24 v84, v84, s9, v141
	v_mad_u32_u24 v85, v85, s9, v141
	v_mad_u32_u24 v86, v86, s9, v141
	v_mad_u32_u24 v87, v87, s9, v141
	v_mad_u32_u24 v88, v88, s9, v141
	v_mad_u32_u24 v89, v89, s9, v141
	v_mad_u32_u24 v90, v90, s9, v141
	v_mad_u32_u24 v91, v91, s9, v141
	v_mad_u32_u24 v92, v92, s9, v141
	v_mad_u32_u24 v93, v93, s9, v141
	v_mad_u32_u24 v94, v94, s9, v141
	v_mad_u32_u24 v95, v95, s9, v141
	v_mad_u32_u24 v96, v96, s9, v141
	v_mad_u32_u24 v97, v97, s9, v141
	v_mad_u32_u24 v98, v98, s9, v141
	v_mad_u32_u24 v99, v99, s9, v141
	v_mad_u32_u24 v100, v100, s9, v141
	v_mad_u32_u24 v101, v101, s9, v141
	v_mad_u32_u24 v102, v102, s9, v141
	v_mad_u32_u24 v103, v103, s9, v141
	v_mad_u32_u24 v104, v104, s9, v141
	v_mad_u32_u24 v105, v105, s9, v141
	v_cmp_gt_u32_e64 s[36:37], s3, v74
	v_cmp_gt_u32_e64 s[38:39], s3, v75
	v_cmp_gt_u32_e64 s[40:41], s3, v76
	v_cmp_gt_u32_e64 s[42:43], s3, v77
	v_cmp_gt_u32_e64 s[44:45], s3, v78
	v_cmp_gt_u32_e64 s[46:47], s3, v79
	v_cmp_gt_u32_e64 s[48:49], s3, v80
	v_cmp_gt_u32_e64 s[50:51], s3, v81
	v_cmp_gt_u32_e64 s[52:53], s3, v82
	v_cmp_gt_u32_e64 s[54:55], s3, v83
	v_cmp_gt_u32_e64 s[56:57], s3, v84
	v_cmp_gt_u32_e64 s[58:59], s3, v85
	v_cmp_gt_u32_e64 s[60:61], s3, v86
	v_cmp_gt_u32_e64 s[62:63], s3, v87
	v_cmp_gt_u32_e64 s[64:65], s3, v88
	v_cmp_gt_u32_e64 s[66:67], s3, v89
	v_cmp_gt_u32_e64 s[68:69], s3, v90
	v_cmp_gt_u32_e64 s[70:71], s3, v91
	v_cmp_gt_u32_e64 s[72:73], s3, v92
	v_cmp_gt_u32_e64 s[74:75], s3, v93
	v_cmp_gt_u32_e64 s[76:77], s3, v94
	v_cmp_gt_u32_e64 s[78:79], s3, v95
	v_cmp_gt_u32_e64 s[80:81], s3, v96
	v_cmp_gt_u32_e64 s[82:83], s3, v97
	v_cmp_gt_u32_e64 s[84:85], s3, v98
	v_cmp_gt_u32_e64 s[86:87], s3, v99
	v_cmp_gt_u32_e64 s[88:89], s3, v100
	v_cmp_gt_u32_e64 s[90:91], s3, v101
	v_cmp_gt_u32_e64 s[92:93], s3, v102
	v_cmp_gt_u32_e64 s[94:95], s3, v103
	v_cmp_gt_u32_e64 s[96:97], s3, v104
	v_cmp_gt_u32_e64 s[98:99], s3, v105
	s_mov_b64 exec, s[36:37]
	ds_add_u32 v74, v142 offset:34816
	s_mov_b64 exec, s[38:39]
	ds_add_u32 v75, v142 offset:34816
	s_mov_b64 exec, s[40:41]
	ds_add_u32 v76, v142 offset:34816
	s_mov_b64 exec, s[42:43]
	ds_add_u32 v77, v142 offset:34816
	s_mov_b64 exec, s[44:45]
	ds_add_u32 v78, v142 offset:34816
	s_mov_b64 exec, s[46:47]
	ds_add_u32 v79, v142 offset:34816
	s_mov_b64 exec, s[48:49]
	ds_add_u32 v80, v142 offset:34816
	s_mov_b64 exec, s[50:51]
	ds_add_u32 v81, v142 offset:34816
	s_mov_b64 exec, s[52:53]
	ds_add_u32 v82, v142 offset:34816
	s_mov_b64 exec, s[54:55]
	ds_add_u32 v83, v142 offset:34816
	s_mov_b64 exec, s[56:57]
	ds_add_u32 v84, v142 offset:34816
	s_mov_b64 exec, s[58:59]
	ds_add_u32 v85, v142 offset:34816
	s_mov_b64 exec, s[60:61]
	ds_add_u32 v86, v142 offset:34816
	s_mov_b64 exec, s[62:63]
	ds_add_u32 v87, v142 offset:34816
	s_mov_b64 exec, s[64:65]
	ds_add_u32 v88, v142 offset:34816
	s_mov_b64 exec, s[66:67]
	ds_add_u32 v89, v142 offset:34816
	s_mov_b64 exec, s[68:69]
	ds_add_u32 v90, v142 offset:34816
	s_mov_b64 exec, s[70:71]
	ds_add_u32 v91, v142 offset:34816
	s_mov_b64 exec, s[72:73]
	ds_add_u32 v92, v142 offset:34816
	s_mov_b64 exec, s[74:75]
	ds_add_u32 v93, v142 offset:34816
	s_mov_b64 exec, s[76:77]
	ds_add_u32 v94, v142 offset:34816
	s_mov_b64 exec, s[78:79]
	ds_add_u32 v95, v142 offset:34816
	s_mov_b64 exec, s[80:81]
	ds_add_u32 v96, v142 offset:34816
	s_mov_b64 exec, s[82:83]
	ds_add_u32 v97, v142 offset:34816
	s_mov_b64 exec, s[84:85]
	ds_add_u32 v98, v142 offset:34816
	s_mov_b64 exec, s[86:87]
	ds_add_u32 v99, v142 offset:34816
	s_mov_b64 exec, s[88:89]
	ds_add_u32 v100, v142 offset:34816
	s_mov_b64 exec, s[90:91]
	ds_add_u32 v101, v142 offset:34816
	s_mov_b64 exec, s[92:93]
	ds_add_u32 v102, v142 offset:34816
	s_mov_b64 exec, s[94:95]
	ds_add_u32 v103, v142 offset:34816
	s_mov_b64 exec, s[96:97]
	ds_add_u32 v104, v142 offset:34816
	s_mov_b64 exec, s[98:99]
	ds_add_u32 v105, v142 offset:34816
	s_mov_b64 exec, -1
	s_waitcnt lgkmcnt(0)
	s_barrier
	v_and_b32_e32 v67, 15, v0
	v_mul_u32_u24_e32 v67, 0x810, v67
	ds_read_b32 v68, v67 offset:34816
	s_waitcnt lgkmcnt(0)
	v_mov_b32_e32 v69, v68
	s_nop 1
	v_add_u32_dpp v69, v69, v69 row_shr:1 row_mask:0xf bank_mask:0xf bound_ctrl:1
	s_nop 1
	v_add_u32_dpp v69, v69, v69 row_shr:2 row_mask:0xf bank_mask:0xf bound_ctrl:1
	s_nop 1
	v_add_u32_dpp v69, v69, v69 row_shr:4 row_mask:0xf bank_mask:0xf bound_ctrl:1
	s_nop 1
	v_add_u32_dpp v69, v69, v69 row_shr:8 row_mask:0xf bank_mask:0xf bound_ctrl:1
	s_nop 1
	v_sub_u32_e32 v70, v69, v68
	v_lshlrev_b32_e32 v70, 2, v70
	v_readlane_b32 s8, v69, 15
	s_cmp_lg_u32 s17, 0
	s_cbranch_scc1 .Lfront_nocursor
	v_cmp_gt_u32_e32 vcc, 16, v1
	s_and_saveexec_b64 s[30:31], vcc
	ds_write_b32 v67, v70 offset:34820
	s_mov_b64 exec, s[30:31]
.Lfront_nocursor:
	s_waitcnt lgkmcnt(0)
	s_barrier
	s_mov_b64 exec, s[36:37]
	ds_add_rtn_u32 v106, v74, v143 offset:34820
	s_mov_b64 exec, s[38:39]
	ds_add_rtn_u32 v107, v75, v143 offset:34820
	s_mov_b64 exec, s[40:41]
	ds_add_rtn_u32 v108, v76, v143 offset:34820
	s_mov_b64 exec, s[42:43]
	ds_add_rtn_u32 v109, v77, v143 offset:34820
	s_mov_b64 exec, s[44:45]
	ds_add_rtn_u32 v110, v78, v143 offset:34820
	s_mov_b64 exec, s[46:47]
	ds_add_rtn_u32 v111, v79, v143 offset:34820
	s_mov_b64 exec, s[48:49]
	ds_add_rtn_u32 v112, v80, v143 offset:34820
	s_mov_b64 exec, s[50:51]
	ds_add_rtn_u32 v113, v81, v143 offset:34820
	s_mov_b64 exec, s[52:53]
	ds_add_rtn_u32 v114, v82, v143 offset:34820
	s_mov_b64 exec, s[54:55]
	ds_add_rtn_u32 v115, v83, v143 offset:34820
	s_mov_b64 exec, s[56:57]
	ds_add_rtn_u32 v116, v84, v143 offset:34820
	s_mov_b64 exec, s[58:59]
	ds_add_rtn_u32 v117, v85, v143 offset:34820
	s_mov_b64 exec, s[60:61]
	ds_add_rtn_u32 v118, v86, v143 offset:34820
	s_mov_b64 exec, s[62:63]
	ds_add_rtn_u32 v119, v87, v143 offset:34820
	s_mov_b64 exec, s[64:65]
	ds_add_rtn_u32 v120, v88, v143 offset:34820
	s_mov_b64 exec, s[66:67]
	ds_add_rtn_u32 v121, v89, v143 offset:34820
	s_mov_b64 exec, s[68:69]
	ds_add_rtn_u32 v122, v90, v143 offset:34820
	s_mov_b64 exec, s[70:71]
	ds_add_rtn_u32 v123, v91, v143 offset:34820
	s_mov_b64 exec, s[72:73]
	ds_add_rtn_u32 v124, v92, v143 offset:34820
	s_mov_b64 exec, s[74:75]
	ds_add_rtn_u32 v125, v93, v143 offset:34820
	s_mov_b64 exec, s[76:77]
	ds_add_rtn_u32 v126, v94, v143 offset:34820
	s_mov_b64 exec, s[78:79]
	ds_add_rtn_u32 v127, v95, v143 offset:34820
	s_mov_b64 exec, s[80:81]
	ds_add_rtn_u32 v128, v96, v143 offset:34820
	s_mov_b64 exec, s[82:83]
	ds_add_rtn_u32 v129, v97, v143 offset:34820
	s_mov_b64 exec, s[84:85]
	ds_add_rtn_u32 v130, v98, v143 offset:34820
	s_mov_b64 exec, s[86:87]
	ds_add_rtn_u32 v131, v99, v143 offset:34820
	s_mov_b64 exec, s[88:89]
	ds_add_rtn_u32 v132, v100, v143 offset:34820
	s_mov_b64 exec, s[90:91]
	ds_add_rtn_u32 v133, v101, v143 offset:34820
	s_mov_b64 exec, s[92:93]
	ds_add_rtn_u32 v134, v102, v143 offset:34820
	s_mov_b64 exec, s[94:95]
	ds_add_rtn_u32 v135, v103, v143 offset:34820
	s_mov_b64 exec, s[96:97]
	ds_add_rtn_u32 v136, v104, v143 offset:34820
	s_mov_b64 exec, s[98:99]
	ds_add_rtn_u32 v137, v105, v143 offset:34820
	s_mov_b64 exec, -1
	v_lshlrev_b32_e32 v145, 18, v0
	v_add_u32_e32 v146, 0x0, v145
	v_or_b32_e32 v74, v146, v74
	v_add_u32_e32 v147, 0x10000, v145
	v_or_b32_e32 v75, v147, v75
	v_add_u32_e32 v146, 0x20000, v145
	v_or_b32_e32 v76, v146, v76
	v_add_u32_e32 v147, 0x30000, v145
	v_or_b32_e32 v77, v147, v77
	v_add_u32_e32 v146, 0x4000000, v145
	v_or_b32_e32 v78, v146, v78
	v_add_u32_e32 v147, 0x4010000, v145
	v_or_b32_e32 v79, v147, v79
	v_add_u32_e32 v146, 0x4020000, v145
	v_or_b32_e32 v80, v146, v80
	v_add_u32_e32 v147, 0x4030000, v145
	v_or_b32_e32 v81, v147, v81
	v_add_u32_e32 v146, 0x8000000, v145
	v_or_b32_e32 v82, v146, v82
	v_add_u32_e32 v147, 0x8010000, v145
	v_or_b32_e32 v83, v147, v83
	v_add_u32_e32 v146, 0x8020000, v145
	v_or_b32_e32 v84, v146, v84
	v_add_u32_e32 v147, 0x8030000, v145
	v_or_b32_e32 v85, v147, v85
	v_add_u32_e32 v146, 0xc000000, v145
	v_or_b32_e32 v86, v146, v86
	v_add_u32_e32 v147, 0xc010000, v145
	v_or_b32_e32 v87, v147, v87
	v_add_u32_e32 v146, 0xc020000, v145
	v_or_b32_e32 v88, v146, v88
	v_add_u32_e32 v147, 0xc030000, v145
	v_or_b32_e32 v89, v147, v89
	v_add_u32_e32 v146, 0x10000000, v145
	v_or_b32_e32 v90, v146, v90
	v_add_u32_e32 v147, 0x10010000, v145
	v_or_b32_e32 v91, v147, v91
	v_add_u32_e32 v146, 0x10020000, v145
	v_or_b32_e32 v92, v146, v92
	v_add_u32_e32 v147, 0x10030000, v145
	v_or_b32_e32 v93, v147, v93
	v_add_u32_e32 v146, 0x14000000, v145
	v_or_b32_e32 v94, v146, v94
	v_add_u32_e32 v147, 0x14010000, v145
	v_or_b32_e32 v95, v147, v95
	v_add_u32_e32 v146, 0x14020000, v145
	v_or_b32_e32 v96, v146, v96
	v_add_u32_e32 v147, 0x14030000, v145
	v_or_b32_e32 v97, v147, v97
	v_add_u32_e32 v146, 0x18000000, v145
	v_or_b32_e32 v98, v146, v98
	v_add_u32_e32 v147, 0x18010000, v145
	v_or_b32_e32 v99, v147, v99
	v_add_u32_e32 v146, 0x18020000, v145
	v_or_b32_e32 v100, v146, v100
	v_add_u32_e32 v147, 0x18030000, v145
	v_or_b32_e32 v101, v147, v101
	v_add_u32_e32 v146, 0x1c000000, v145
	v_or_b32_e32 v102, v146, v102
	v_add_u32_e32 v147, 0x1c010000, v145
	v_or_b32_e32 v103, v147, v103
	v_add_u32_e32 v146, 0x1c020000, v145
	v_or_b32_e32 v104, v146, v104
	v_add_u32_e32 v147, 0x1c030000, v145
	v_or_b32_e32 v105, v147, v105
	s_waitcnt lgkmcnt(0)
	s_mov_b64 exec, s[36:37]
	ds_write_b32 v106, v74
	s_mov_b64 exec, s[38:39]
	ds_write_b32 v107, v75
	s_mov_b64 exec, s[40:41]
	ds_write_b32 v108, v76
	s_mov_b64 exec, s[42:43]
	ds_write_b32 v109, v77
	s_mov_b64 exec, s[44:45]
	ds_write_b32 v110, v78
	s_mov_b64 exec, s[46:47]
	ds_write_b32 v111, v79
	s_mov_b64 exec, s[48:49]
	ds_write_b32 v112, v80
	s_mov_b64 exec, s[50:51]
	ds_write_b32 v113, v81
	s_mov_b64 exec, s[52:53]
	ds_write_b32 v114, v82
	s_mov_b64 exec, s[54:55]
	ds_write_b32 v115, v83
	s_mov_b64 exec, s[56:57]
	ds_write_b32 v116, v84
	s_mov_b64 exec, s[58:59]
	ds_write_b32 v117, v85
	s_mov_b64 exec, s[60:61]
	ds_write_b32 v118, v86
	s_mov_b64 exec, s[62:63]
	ds_write_b32 v119, v87
	s_mov_b64 exec, s[64:65]
	ds_write_b32 v120, v88
	s_mov_b64 exec, s[66:67]
	ds_write_b32 v121, v89
	s_mov_b64 exec, s[68:69]
	ds_write_b32 v122, v90
	s_mov_b64 exec, s[70:71]
	ds_write_b32 v123, v91
	s_mov_b64 exec, s[72:73]
	ds_write_b32 v124, v92
	s_mov_b64 exec, s[74:75]
	ds_write_b32 v125, v93
	s_mov_b64 exec, s[76:77]
	ds_write_b32 v126, v94
	s_mov_b64 exec, s[78:79]
	ds_write_b32 v127, v95
	s_mov_b64 exec, s[80:81]
	ds_write_b32 v128, v96
	s_mov_b64 exec, s[82:83]
	ds_write_b32 v129, v97
	s_mov_b64 exec, s[84:85]
	ds_write_b32 v130, v98
	s_mov_b64 exec, s[86:87]
	ds_write_b32 v131, v99
	s_mov_b64 exec, s[88:89]
	ds_write_b32 v132, v100
	s_mov_b64 exec, s[90:91]
	ds_write_b32 v133, v101
	s_mov_b64 exec, s[92:93]
	ds_write_b32 v134, v102
	s_mov_b64 exec, s[94:95]
	ds_write_b32 v135, v103
	s_mov_b64 exec, s[96:97]
	ds_write_b32 v136, v104
	s_mov_b64 exec, s[98:99]
	ds_write_b32 v137, v105
	s_mov_b64 exec, -1
	s_waitcnt lgkmcnt(0)
	s_barrier
	v_and_b32_e32 v150, 15, v0
	v_or_b32_e32 v150, s24, v150
	v_and_b32_e32 v151, 48, v0
	v_lshl_or_b32 v150, v150, 10, v151
	global_load_dwordx4 v[62:65], v150, s[22:23] offset:0
	global_load_dwordx4 v[58:61], v150, s[22:23] offset:64
	global_load_dwordx4 v[54:57], v150, s[22:23] offset:128
	global_load_dwordx4 v[50:53], v150, s[22:23] offset:192
	global_load_dwordx4 v[46:49], v150, s[22:23] offset:256
	global_load_dwordx4 v[42:45], v150, s[22:23] offset:320
	global_load_dwordx4 v[38:41], v150, s[22:23] offset:384
	global_load_dwordx4 v[34:37], v150, s[22:23] offset:448
	global_load_dwordx4 v[30:33], v150, s[22:23] offset:512
	global_load_dwordx4 v[26:29], v150, s[22:23] offset:576
	global_load_dwordx4 v[22:25], v150, s[22:23] offset:640
	global_load_dwordx4 v[18:21], v150, s[22:23] offset:704
	global_load_dwordx4 v[14:17], v150, s[22:23] offset:768
	global_load_dwordx4 v[10:13], v150, s[22:23] offset:832
	global_load_dwordx4 v[6:9], v150, s[22:23] offset:896
	global_load_dwordx4 v[2:5], v150, s[22:23] offset:960
	v_lshlrev_b32_e32 v218, 4, v1
	v_lshlrev_b32_e32 v219, 3, v1
	v_mov_b32_e32 v223, 0x11540
	v_bfrev_b32_e32 v199, 1
	v_mov_b32_e32 v198, 1
	v_and_b32_e32 v221, 15, v1
	v_mov_b32_e32 v200, 0
	v_mov_b32_e32 v201, 0
	v_mov_b32_e32 v202, 0
	v_mov_b32_e32 v203, 0
	v_mov_b32_e32 v204, 0
	v_mov_b32_e32 v205, 0
	v_mov_b32_e32 v206, 0
	v_mov_b32_e32 v207, 0
	s_mov_b32 s50, -1
	s_branch .Lg0_start
